# grid barrier: early L2 write-backs by the 17th and 29th arrivers of each XCD
# baseline (speedup 1.0000x reference)
.LBB0_265:
	v_readlane_b32 s4, v254, 37
	s_lshl_b32 s4, s4, 2
	s_add_u32 s25, s2, s4
	s_addc_u32 s24, s3, 0
	v_mov_b32_e32 v1, s25
	v_add_co_u32_e32 v4, vcc, 0x1000, v1
	v_mov_b32_e32 v1, s24
	s_nop 0
	v_addc_co_u32_e32 v5, vcc, 0, v1, vcc
	flat_atomic_add v3, v[4:5], v193 offset:1024 sc0
	v_cvt_f32_u32_e32 v1, v2
	v_sub_u32_e32 v4, 0, v2
	v_rcp_iflag_f32_e32 v1, v1
	s_nop 0
	v_mul_f32_e32 v1, 0x4f7ffffe, v1
	v_cvt_u32_f32_e32 v1, v1
	v_mul_lo_u32 v4, v4, v1
	v_mul_hi_u32 v4, v1, v4
	v_add_u32_e32 v1, v1, v4
	s_waitcnt vmcnt(0) lgkmcnt(0)
	v_and_b32_e32 v5, 31, v3
	v_cmp_eq_u32_e32 vcc, 16, v5
	v_cmp_eq_u32_e64 s[100:101], 28, v5
	s_nop 1
	s_or_b64 vcc, vcc, s[100:101]
	s_nop 4
	s_cbranch_vccz .Lhalf_flush_11
	buffer_wbl2 sc1

.LBB0_353:
	v_readlane_b32 s4, v254, 37
	s_lshl_b32 s4, s4, 2
	s_add_u32 s27, s2, s4
	s_addc_u32 s26, s3, 0
	v_mov_b32_e32 v1, s27
	v_add_co_u32_e32 v4, vcc, 0x1000, v1
	v_mov_b32_e32 v1, s26
	s_nop 0
	v_addc_co_u32_e32 v5, vcc, 0, v1, vcc
	flat_atomic_add v3, v[4:5], v193 offset:1024 sc0
	v_cvt_f32_u32_e32 v1, v2
	v_sub_u32_e32 v4, 0, v2
	v_rcp_iflag_f32_e32 v1, v1
	s_nop 0
	v_mul_f32_e32 v1, 0x4f7ffffe, v1
	v_cvt_u32_f32_e32 v1, v1
	v_mul_lo_u32 v4, v4, v1
	v_mul_hi_u32 v4, v1, v4
	v_add_u32_e32 v1, v1, v4
	s_waitcnt vmcnt(0) lgkmcnt(0)
	v_and_b32_e32 v5, 31, v3
	v_cmp_eq_u32_e32 vcc, 16, v5
	v_cmp_eq_u32_e64 s[100:101], 28, v5
	s_nop 1
	s_or_b64 vcc, vcc, s[100:101]
	s_nop 4
	s_cbranch_vccz .Lhalf_flush_10
	buffer_wbl2 sc1

.LBB0_583:
	v_readlane_b32 s6, v254, 37
	s_lshl_b32 s6, s6, 2
	s_add_u32 s30, s2, s6
	s_addc_u32 s29, s3, 0
	v_mov_b32_e32 v1, s30
	v_add_co_u32_e32 v4, vcc, 0x1000, v1
	v_mov_b32_e32 v1, s29
	s_nop 0
	v_addc_co_u32_e32 v5, vcc, 0, v1, vcc
	flat_atomic_add v3, v[4:5], v193 offset:1024 sc0
	v_cvt_f32_u32_e32 v1, v2
	v_sub_u32_e32 v4, 0, v2
	v_rcp_iflag_f32_e32 v1, v1
	s_nop 0
	v_mul_f32_e32 v1, 0x4f7ffffe, v1
	v_cvt_u32_f32_e32 v1, v1
	v_mul_lo_u32 v4, v4, v1
	v_mul_hi_u32 v4, v1, v4
	v_add_u32_e32 v1, v1, v4
	s_waitcnt vmcnt(0) lgkmcnt(0)
	v_and_b32_e32 v5, 31, v3
	v_cmp_eq_u32_e32 vcc, 16, v5
	v_cmp_eq_u32_e64 s[100:101], 28, v5
	s_nop 1
	s_or_b64 vcc, vcc, s[100:101]
	s_nop 4
	s_cbranch_vccz .Lhalf_flush_7
	buffer_wbl2 sc1

.LBB0_689:
	v_readlane_b32 s4, v254, 37
	s_lshl_b32 s4, s4, 2
	s_add_u32 s9, s2, s4
	s_addc_u32 s8, s3, 0
	v_mov_b32_e32 v1, s9
	v_add_co_u32_e32 v4, vcc, 0x1000, v1
	v_mov_b32_e32 v1, s8
	s_nop 0
	v_addc_co_u32_e32 v5, vcc, 0, v1, vcc
	flat_atomic_add v3, v[4:5], v193 offset:1024 sc0
	v_cvt_f32_u32_e32 v1, v2
	v_sub_u32_e32 v4, 0, v2
	v_rcp_iflag_f32_e32 v1, v1
	s_nop 0
	v_mul_f32_e32 v1, 0x4f7ffffe, v1
	v_cvt_u32_f32_e32 v1, v1
	v_mul_lo_u32 v4, v4, v1
	v_mul_hi_u32 v4, v1, v4
	v_add_u32_e32 v1, v1, v4
	s_waitcnt vmcnt(0) lgkmcnt(0)
	v_and_b32_e32 v5, 31, v3
	v_cmp_eq_u32_e32 vcc, 16, v5
	v_cmp_eq_u32_e64 s[100:101], 28, v5
	s_nop 1
	s_or_b64 vcc, vcc, s[100:101]
	s_nop 4
	s_cbranch_vccz .Lhalf_flush_6
	buffer_wbl2 sc1
